# removed spurious vmcnt(0) in gate/up unit header; peeled first K-iteration of both fp8 GEMM loops (MFMA C=0) so the 128-register accumulator zeroing disappears
# speedup vs baseline: 1.0136x; 1.0136x over previous
.LBB0_48:
	s_ashr_i32 s51, s50, 31
	s_lshl_b64 s[58:59], s[50:51], 18
	s_add_u32 s58, s14, s58
	s_addc_u32 s59, s15, s59
	s_and_b64 s[60:61], s[54:55], exec
	s_cselect_b32 s6, s59, s27
	s_cselect_b32 s51, s58, s26
	s_ashr_i32 s53, s52, 31
	s_lshl_b64 s[60:61], s[52:53], 20
	s_add_u32 s4, s16, s60
	s_addc_u32 s53, s17, s61
	s_ashr_i32 s49, s48, 31
	s_lshl_b64 s[60:61], s[48:49], 18
	s_add_u32 s60, s4, s60
	s_addc_u32 s61, s53, s61
	s_and_b64 s[68:69], s[54:55], exec
	s_cselect_b32 s49, s61, s37
	s_cselect_b32 s53, s60, s36
	s_add_u32 s26, s26, 0x20080
	s_addc_u32 s27, s27, 0
	s_add_u32 s65, s36, 0x100
	s_addc_u32 s74, s37, 0
	s_mov_b32 s92, -2
	s_add_u32 s36, s26, 0xfffe0080
	s_addc_u32 s37, s27, -1
	s_add_i32 s4, 0, 0x10000
	s_cmp_eq_u32 s92, 4
	s_cselect_b32 s69, s6, s37
	s_cselect_b32 s68, s51, s36
	s_cselect_b32 s37, s49, s74
	s_cselect_b32 s36, s53, s65
	s_add_i32 s93, 0, 0x14000
	v_add_u32_e32 v2, s4, v184
	v_add_u32_e32 v14, s93, v184
	ds_read_b128 v[18:21], v2
	ds_read_b128 v[22:25], v2 offset:1024
	ds_read_b128 v[26:29], v2 offset:2048
	ds_read_b128 v[30:33], v2 offset:3072
	ds_read_b128 v[2:5], v14
	ds_read_b128 v[6:9], v14 offset:1024
	ds_read_b128 v[10:13], v14 offset:2048
	ds_read_b128 v[14:17], v14 offset:3072
	v_lshl_add_u64 v[188:189], s[26:27], 0, v[170:171]
	s_add_i32 m0, s63, 0xc000
	ds_read_b128 v[174:177], v187
	ds_read_b128 v[178:181], v187 offset:1024
	ds_read_b128 v[196:199], v187 offset:2048
	ds_read_b128 v[200:203], v187 offset:3072
	ds_read_b128 v[204:207], v187 offset:4096
	ds_read_b128 v[208:211], v187 offset:5120
	ds_read_b128 v[212:215], v187 offset:6144
	ds_read_b128 v[216:219], v187 offset:7168
	global_load_lds_dwordx4 v[188:189], off
	v_lshl_add_u64 v[188:189], s[26:27], 0, v[172:173]
	s_add_i32 m0, s63, 0xe000
	s_nop 0
	global_load_lds_dwordx4 v[188:189], off
	s_waitcnt vmcnt(8)
	s_waitcnt lgkmcnt(0)
	s_barrier
	s_setprio 1
	s_waitcnt lgkmcnt(0)
	v_mfma_scale_f32_16x16x128_f8f6f4 v[158:161], v[18:25], v[174:181], 0, v191, v191 op_sel_hi:[0,0,0]
	v_mfma_scale_f32_16x16x128_f8f6f4 v[154:157], v[26:33], v[174:181], 0, v191, v191 op_sel_hi:[0,0,0]
	v_mfma_scale_f32_16x16x128_f8f6f4 v[150:153], v[18:25], v[196:203], 0, v191, v191 op_sel_hi:[0,0,0]
	v_mfma_scale_f32_16x16x128_f8f6f4 v[146:149], v[26:33], v[196:203], 0, v191, v191 op_sel_hi:[0,0,0]
	v_mfma_scale_f32_16x16x128_f8f6f4 v[126:129], v[18:25], v[204:211], 0, v191, v191 op_sel_hi:[0,0,0]
	v_mfma_scale_f32_16x16x128_f8f6f4 v[122:125], v[26:33], v[204:211], 0, v191, v191 op_sel_hi:[0,0,0]
	v_mfma_scale_f32_16x16x128_f8f6f4 v[118:121], v[18:25], v[212:219], 0, v191, v191 op_sel_hi:[0,0,0]
	v_mfma_scale_f32_16x16x128_f8f6f4 v[114:117], v[26:33], v[212:219], 0, v191, v191 op_sel_hi:[0,0,0]
	s_setprio 0
	s_setprio 1
	v_mfma_scale_f32_16x16x128_f8f6f4 v[142:145], v[2:9], v[174:181], 0, v191, v191 op_sel_hi:[0,0,0]
	v_mfma_scale_f32_16x16x128_f8f6f4 v[138:141], v[10:17], v[174:181], 0, v191, v191 op_sel_hi:[0,0,0]
	v_mfma_scale_f32_16x16x128_f8f6f4 v[134:137], v[2:9], v[196:203], 0, v191, v191 op_sel_hi:[0,0,0]
	v_mfma_scale_f32_16x16x128_f8f6f4 v[130:133], v[10:17], v[196:203], 0, v191, v191 op_sel_hi:[0,0,0]
	v_mfma_scale_f32_16x16x128_f8f6f4 v[110:113], v[2:9], v[204:211], 0, v191, v191 op_sel_hi:[0,0,0]
	v_mfma_scale_f32_16x16x128_f8f6f4 v[106:109], v[10:17], v[204:211], 0, v191, v191 op_sel_hi:[0,0,0]
	v_mfma_scale_f32_16x16x128_f8f6f4 v[102:105], v[2:9], v[212:219], 0, v191, v191 op_sel_hi:[0,0,0]
	v_mfma_scale_f32_16x16x128_f8f6f4 v[98:101], v[10:17], v[212:219], 0, v191, v191 op_sel_hi:[0,0,0]
	s_setprio 0
	s_barrier
	s_add_i32 s4, s4, s45
	v_lshl_add_u64 v[174:175], s[36:37], 0, v[0:1]
	s_mov_b32 m0, s4
	ds_read_b128 v[196:199], v187 offset:16384
	ds_read_b128 v[200:203], v187 offset:17408
	ds_read_b128 v[204:207], v187 offset:18432
	ds_read_b128 v[208:211], v187 offset:19456
	ds_read_b128 v[212:215], v187 offset:20480
	ds_read_b128 v[216:219], v187 offset:21504
	ds_read_b128 v[234:237], v187 offset:22528
	ds_read_b128 v[238:241], v187 offset:23552
	global_load_lds_dwordx4 v[174:175], off
	s_add_i32 m0, s4, 0x2000
	s_add_u32 s86, s36, 0x20000
	v_lshl_add_u64 v[176:177], s[36:37], 0, v[166:167]
	s_addc_u32 s87, s37, 0
	s_add_i32 s4, s93, s45
	global_load_lds_dwordx4 v[176:177], off
	v_lshl_add_u64 v[178:179], s[86:87], 0, v[0:1]
	s_mov_b32 m0, s4
	v_lshl_add_u64 v[180:181], s[68:69], 0, v[164:165]
	global_load_lds_dwordx4 v[178:179], off
	v_lshl_add_u64 v[178:179], s[86:87], 0, v[166:167]
	s_add_i32 m0, s4, 0x2000
	s_nop 0
	global_load_lds_dwordx4 v[178:179], off
	v_lshl_add_u64 v[178:179], s[68:69], 0, v[162:163]
	s_mov_b32 m0, s63
	s_nop 0
	global_load_lds_dwordx4 v[178:179], off
	s_mov_b32 m0, s67
	s_nop 0
	global_load_lds_dwordx4 v[180:181], off
	s_waitcnt vmcnt(8)
	s_waitcnt lgkmcnt(0)
	s_barrier
	s_setprio 1
	s_waitcnt lgkmcnt(0)
	v_mfma_scale_f32_16x16x128_f8f6f4 v[94:97], v[18:25], v[196:203], 0, v191, v191 op_sel_hi:[0,0,0]
	v_mfma_scale_f32_16x16x128_f8f6f4 v[90:93], v[26:33], v[196:203], 0, v191, v191 op_sel_hi:[0,0,0]
	v_mfma_scale_f32_16x16x128_f8f6f4 v[86:89], v[18:25], v[204:211], 0, v191, v191 op_sel_hi:[0,0,0]
	v_mfma_scale_f32_16x16x128_f8f6f4 v[82:85], v[26:33], v[204:211], 0, v191, v191 op_sel_hi:[0,0,0]
	v_mfma_scale_f32_16x16x128_f8f6f4 v[62:65], v[18:25], v[212:219], 0, v191, v191 op_sel_hi:[0,0,0]
	v_mfma_scale_f32_16x16x128_f8f6f4 v[58:61], v[26:33], v[212:219], 0, v191, v191 op_sel_hi:[0,0,0]
	v_mfma_scale_f32_16x16x128_f8f6f4 v[54:57], v[18:25], v[234:241], 0, v191, v191 op_sel_hi:[0,0,0]
	v_mfma_scale_f32_16x16x128_f8f6f4 v[50:53], v[26:33], v[234:241], 0, v191, v191 op_sel_hi:[0,0,0]
	s_setprio 0
	s_setprio 1
	v_mfma_scale_f32_16x16x128_f8f6f4 v[78:81], v[2:9], v[196:203], 0, v191, v191 op_sel_hi:[0,0,0]
	v_mfma_scale_f32_16x16x128_f8f6f4 v[74:77], v[10:17], v[196:203], 0, v191, v191 op_sel_hi:[0,0,0]
	v_mfma_scale_f32_16x16x128_f8f6f4 v[70:73], v[2:9], v[204:211], 0, v191, v191 op_sel_hi:[0,0,0]
	v_mfma_scale_f32_16x16x128_f8f6f4 v[66:69], v[10:17], v[204:211], 0, v191, v191 op_sel_hi:[0,0,0]
	v_mfma_scale_f32_16x16x128_f8f6f4 v[46:49], v[2:9], v[212:219], 0, v191, v191 op_sel_hi:[0,0,0]
	v_mfma_scale_f32_16x16x128_f8f6f4 v[42:45], v[10:17], v[212:219], 0, v191, v191 op_sel_hi:[0,0,0]
	v_mfma_scale_f32_16x16x128_f8f6f4 v[38:41], v[2:9], v[234:241], 0, v191, v191 op_sel_hi:[0,0,0]
	v_mfma_scale_f32_16x16x128_f8f6f4 v[34:37], v[10:17], v[234:241], 0, v191, v191 op_sel_hi:[0,0,0]
	s_setprio 0
	s_barrier
	s_add_i32 s4, 0, 0x18000
	s_add_i32 s86, 0, 0x1c000
	v_add_u32_e32 v14, s4, v184
	v_add_u32_e32 v30, s86, v184
	ds_read_b128 v[2:5], v14
	ds_read_b128 v[6:9], v14 offset:1024
	ds_read_b128 v[10:13], v14 offset:2048
	ds_read_b128 v[14:17], v14 offset:3072
	ds_read_b128 v[18:21], v30
	ds_read_b128 v[22:25], v30 offset:1024
	ds_read_b128 v[26:29], v30 offset:2048
	ds_read_b128 v[30:33], v30 offset:3072
	s_add_u32 s68, s68, 0x20000
	s_addc_u32 s69, s69, 0
	s_mov_b32 m0, s73
	v_lshl_add_u64 v[188:189], s[68:69], 0, v[162:163]
	ds_read_b128 v[196:199], v187 offset:32768
	ds_read_b128 v[200:203], v187 offset:33792
	ds_read_b128 v[204:207], v187 offset:34816
	ds_read_b128 v[208:211], v187 offset:35840
	ds_read_b128 v[212:215], v187 offset:36864
	ds_read_b128 v[216:219], v187 offset:37888
	ds_read_b128 v[234:237], v187 offset:38912
	ds_read_b128 v[238:241], v187 offset:39936
	global_load_lds_dwordx4 v[188:189], off
	v_lshl_add_u64 v[188:189], s[68:69], 0, v[164:165]
	s_mov_b32 m0, s75
	s_nop 0
	global_load_lds_dwordx4 v[188:189], off
	s_waitcnt vmcnt(8)
	s_waitcnt lgkmcnt(0)
	s_barrier
	s_setprio 1
	s_waitcnt lgkmcnt(0)
	v_mfma_scale_f32_16x16x128_f8f6f4 v[158:161], v[2:9], v[196:203], v[158:161], v191, v191 op_sel_hi:[0,0,0]
	v_mfma_scale_f32_16x16x128_f8f6f4 v[154:157], v[10:17], v[196:203], v[154:157], v191, v191 op_sel_hi:[0,0,0]
	v_mfma_scale_f32_16x16x128_f8f6f4 v[150:153], v[2:9], v[204:211], v[150:153], v191, v191 op_sel_hi:[0,0,0]
	v_mfma_scale_f32_16x16x128_f8f6f4 v[146:149], v[10:17], v[204:211], v[146:149], v191, v191 op_sel_hi:[0,0,0]
	v_mfma_scale_f32_16x16x128_f8f6f4 v[126:129], v[2:9], v[212:219], v[126:129], v191, v191 op_sel_hi:[0,0,0]
	v_mfma_scale_f32_16x16x128_f8f6f4 v[122:125], v[10:17], v[212:219], v[122:125], v191, v191 op_sel_hi:[0,0,0]
	v_mfma_scale_f32_16x16x128_f8f6f4 v[118:121], v[2:9], v[234:241], v[118:121], v191, v191 op_sel_hi:[0,0,0]
	v_mfma_scale_f32_16x16x128_f8f6f4 v[114:117], v[10:17], v[234:241], v[114:117], v191, v191 op_sel_hi:[0,0,0]
	s_setprio 0
	s_setprio 1
	v_mfma_scale_f32_16x16x128_f8f6f4 v[142:145], v[18:25], v[196:203], v[142:145], v191, v191 op_sel_hi:[0,0,0]
	v_mfma_scale_f32_16x16x128_f8f6f4 v[138:141], v[26:33], v[196:203], v[138:141], v191, v191 op_sel_hi:[0,0,0]
	v_mfma_scale_f32_16x16x128_f8f6f4 v[134:137], v[18:25], v[204:211], v[134:137], v191, v191 op_sel_hi:[0,0,0]
	v_mfma_scale_f32_16x16x128_f8f6f4 v[130:133], v[26:33], v[204:211], v[130:133], v191, v191 op_sel_hi:[0,0,0]
	v_mfma_scale_f32_16x16x128_f8f6f4 v[110:113], v[18:25], v[212:219], v[110:113], v191, v191 op_sel_hi:[0,0,0]
	v_mfma_scale_f32_16x16x128_f8f6f4 v[106:109], v[26:33], v[212:219], v[106:109], v191, v191 op_sel_hi:[0,0,0]
	v_mfma_scale_f32_16x16x128_f8f6f4 v[102:105], v[18:25], v[234:241], v[102:105], v191, v191 op_sel_hi:[0,0,0]
	v_mfma_scale_f32_16x16x128_f8f6f4 v[98:101], v[26:33], v[234:241], v[98:101], v191, v191 op_sel_hi:[0,0,0]
	s_setprio 0
	s_barrier
	s_add_i32 s4, s4, s45
	v_lshl_add_u64 v[174:175], v[174:175], 0, s[22:23]
	s_mov_b32 m0, s4
	ds_read_b128 v[196:199], v187 offset:49152
	ds_read_b128 v[200:203], v187 offset:50176
	ds_read_b128 v[204:207], v187 offset:51200
	ds_read_b128 v[208:211], v187 offset:52224
	ds_read_b128 v[212:215], v187 offset:53248
	ds_read_b128 v[216:219], v187 offset:54272
	ds_read_b128 v[234:237], v187 offset:55296
	ds_read_b128 v[238:241], v187 offset:56320
	global_load_lds_dwordx4 v[174:175], off
	s_add_i32 m0, s4, 0x2000
	s_add_u32 s36, s36, 0x20080
	v_lshl_add_u64 v[174:175], v[176:177], 0, s[22:23]
	s_addc_u32 s37, s37, 0
	s_add_i32 s4, s86, s45
	global_load_lds_dwordx4 v[174:175], off
	v_lshl_add_u64 v[174:175], s[36:37], 0, v[0:1]
	s_mov_b32 m0, s4
	s_nop 0
	global_load_lds_dwordx4 v[174:175], off
	v_lshl_add_u64 v[174:175], s[36:37], 0, v[166:167]
	s_add_i32 m0, s4, 0x2000
	s_nop 0
	global_load_lds_dwordx4 v[174:175], off
	v_lshl_add_u64 v[174:175], v[178:179], 0, s[22:23]
	s_mov_b32 m0, s79
	s_nop 0
	global_load_lds_dwordx4 v[174:175], off
	v_lshl_add_u64 v[174:175], v[180:181], 0, s[22:23]
	s_mov_b32 m0, s82
	s_nop 0
	global_load_lds_dwordx4 v[174:175], off
	s_waitcnt vmcnt(8)
	s_waitcnt lgkmcnt(0)
	s_barrier
	s_setprio 1
	s_waitcnt lgkmcnt(0)
	v_mfma_scale_f32_16x16x128_f8f6f4 v[94:97], v[2:9], v[196:203], v[94:97], v191, v191 op_sel_hi:[0,0,0]
	v_mfma_scale_f32_16x16x128_f8f6f4 v[90:93], v[10:17], v[196:203], v[90:93], v191, v191 op_sel_hi:[0,0,0]
	v_mfma_scale_f32_16x16x128_f8f6f4 v[86:89], v[2:9], v[204:211], v[86:89], v191, v191 op_sel_hi:[0,0,0]
	v_mfma_scale_f32_16x16x128_f8f6f4 v[82:85], v[10:17], v[204:211], v[82:85], v191, v191 op_sel_hi:[0,0,0]
	v_mfma_scale_f32_16x16x128_f8f6f4 v[62:65], v[2:9], v[212:219], v[62:65], v191, v191 op_sel_hi:[0,0,0]
	v_mfma_scale_f32_16x16x128_f8f6f4 v[58:61], v[10:17], v[212:219], v[58:61], v191, v191 op_sel_hi:[0,0,0]
	v_mfma_scale_f32_16x16x128_f8f6f4 v[54:57], v[2:9], v[234:241], v[54:57], v191, v191 op_sel_hi:[0,0,0]
	v_mfma_scale_f32_16x16x128_f8f6f4 v[50:53], v[10:17], v[234:241], v[50:53], v191, v191 op_sel_hi:[0,0,0]
	s_setprio 0
	s_setprio 1
	v_mfma_scale_f32_16x16x128_f8f6f4 v[78:81], v[18:25], v[196:203], v[78:81], v191, v191 op_sel_hi:[0,0,0]
	v_mfma_scale_f32_16x16x128_f8f6f4 v[74:77], v[26:33], v[196:203], v[74:77], v191, v191 op_sel_hi:[0,0,0]
	v_mfma_scale_f32_16x16x128_f8f6f4 v[70:73], v[18:25], v[204:211], v[70:73], v191, v191 op_sel_hi:[0,0,0]
	v_mfma_scale_f32_16x16x128_f8f6f4 v[66:69], v[26:33], v[204:211], v[66:69], v191, v191 op_sel_hi:[0,0,0]
	v_mfma_scale_f32_16x16x128_f8f6f4 v[46:49], v[18:25], v[212:219], v[46:49], v191, v191 op_sel_hi:[0,0,0]
	v_mfma_scale_f32_16x16x128_f8f6f4 v[42:45], v[26:33], v[212:219], v[42:45], v191, v191 op_sel_hi:[0,0,0]
	v_mfma_scale_f32_16x16x128_f8f6f4 v[38:41], v[18:25], v[234:241], v[38:41], v191, v191 op_sel_hi:[0,0,0]
	v_mfma_scale_f32_16x16x128_f8f6f4 v[34:37], v[26:33], v[234:241], v[34:37], v191, v191 op_sel_hi:[0,0,0]
	s_setprio 0
	s_barrier
	s_add_i32 s92, s92, 2
	s_add_u32 s26, s26, 0x100
	s_addc_u32 s27, s27, 0
	s_add_u32 s65, s65, 0x100
	s_addc_u32 s74, s74, 0

.LBB0_248:
	s_ashr_i32 s63, s62, 31
	s_lshl_b64 s[36:37], s[62:63], 21
	s_add_u32 s4, s82, s36
	s_addc_u32 s6, s83, s37
	s_ashr_i32 s61, s60, 31
	s_lshl_b64 s[36:37], s[60:61], 18
	s_add_u32 s64, s4, s36
	s_addc_u32 s65, s6, s37
	s_and_b64 s[36:37], s[70:71], exec
	s_cselect_b32 s6, s65, s27
	s_cselect_b32 s31, s64, s26
	v_mov_b32_e32 v173, v1
	v_mov_b32_e32 v175, v1
	s_add_u32 s61, s26, 0x100
	v_lshl_add_u64 v[176:177], s[54:55], 0, v[174:175]
	v_lshl_add_u64 v[178:179], s[54:55], 0, v[172:173]
	s_addc_u32 s63, s27, 0
	s_mov_b32 s67, -2
	s_mov_b64 s[26:27], 0
	s_add_u32 s4, s46, s26
	s_addc_u32 s36, s47, s27
	s_add_u32 s69, s4, 0x2e000100
	s_addc_u32 s70, s36, 0
	s_add_u32 s74, s61, s26
	s_addc_u32 s86, s63, s27
	s_add_i32 s4, 0, 0x10000
	s_cmpk_eq_i32 s26, 0x300
	s_cselect_b64 vcc, -1, 0
	s_and_b64 s[36:37], vcc, exec
	s_cselect_b32 s71, s41, s70
	s_cselect_b32 s70, s40, s69
	v_add_u32_e32 v0, s4, v200
	s_cselect_b32 s37, s6, s86
	s_cselect_b32 s36, s31, s74
	s_add_i32 s69, 0, 0x14000
	ds_read_b128 v[18:21], v0
	ds_read_b128 v[22:25], v0 offset:1024
	ds_read_b128 v[26:29], v0 offset:2048
	ds_read_b128 v[30:33], v0 offset:3072
	v_add_u32_e32 v0, s69, v200
	ds_read_b128 v[2:5], v0
	ds_read_b128 v[6:9], v0 offset:1024
	ds_read_b128 v[10:13], v0 offset:2048
	ds_read_b128 v[14:17], v0 offset:3072
	v_lshl_add_u64 v[222:223], v[178:179], 0, s[26:27]
	s_add_i32 m0, s93, 0xc000
	ds_read_b128 v[180:183], v201
	ds_read_b128 v[184:187], v201 offset:1024
	ds_read_b128 v[206:209], v201 offset:2048
	ds_read_b128 v[210:213], v201 offset:3072
	ds_read_b128 v[214:217], v201 offset:4096
	ds_read_b128 v[218:221], v201 offset:5120
	ds_read_b128 v[234:237], v201 offset:6144
	ds_read_b128 v[238:241], v201 offset:7168
	global_load_lds_dwordx4 v[222:223], off
	v_lshl_add_u64 v[222:223], v[176:177], 0, s[26:27]
	s_add_i32 m0, s93, 0xe000
	s_nop 0
	global_load_lds_dwordx4 v[222:223], off
	s_waitcnt vmcnt(8)
	s_waitcnt lgkmcnt(0)
	s_barrier
	s_setprio 1
	s_waitcnt lgkmcnt(0)
	v_mfma_scale_f32_16x16x128_f8f6f4 v[158:161], v[18:25], v[180:187], 0, v191, v191 op_sel_hi:[0,0,0]
	v_mfma_scale_f32_16x16x128_f8f6f4 v[154:157], v[26:33], v[180:187], 0, v191, v191 op_sel_hi:[0,0,0]
	v_mfma_scale_f32_16x16x128_f8f6f4 v[142:145], v[18:25], v[206:213], 0, v191, v191 op_sel_hi:[0,0,0]
	v_mfma_scale_f32_16x16x128_f8f6f4 v[138:141], v[26:33], v[206:213], 0, v191, v191 op_sel_hi:[0,0,0]
	v_mfma_scale_f32_16x16x128_f8f6f4 v[126:129], v[18:25], v[214:221], 0, v191, v191 op_sel_hi:[0,0,0]
	v_mfma_scale_f32_16x16x128_f8f6f4 v[122:125], v[26:33], v[214:221], 0, v191, v191 op_sel_hi:[0,0,0]
	v_mfma_scale_f32_16x16x128_f8f6f4 v[110:113], v[18:25], v[234:241], 0, v191, v191 op_sel_hi:[0,0,0]
	v_mfma_scale_f32_16x16x128_f8f6f4 v[106:109], v[26:33], v[234:241], 0, v191, v191 op_sel_hi:[0,0,0]
	s_setprio 0
	s_setprio 1
	v_mfma_scale_f32_16x16x128_f8f6f4 v[150:153], v[2:9], v[180:187], 0, v191, v191 op_sel_hi:[0,0,0]
	v_mfma_scale_f32_16x16x128_f8f6f4 v[146:149], v[10:17], v[180:187], 0, v191, v191 op_sel_hi:[0,0,0]
	v_mfma_scale_f32_16x16x128_f8f6f4 v[134:137], v[2:9], v[206:213], 0, v191, v191 op_sel_hi:[0,0,0]
	v_mfma_scale_f32_16x16x128_f8f6f4 v[130:133], v[10:17], v[206:213], 0, v191, v191 op_sel_hi:[0,0,0]
	v_mfma_scale_f32_16x16x128_f8f6f4 v[118:121], v[2:9], v[214:221], 0, v191, v191 op_sel_hi:[0,0,0]
	v_mfma_scale_f32_16x16x128_f8f6f4 v[114:117], v[10:17], v[214:221], 0, v191, v191 op_sel_hi:[0,0,0]
	v_mfma_scale_f32_16x16x128_f8f6f4 v[102:105], v[2:9], v[234:241], 0, v191, v191 op_sel_hi:[0,0,0]
	v_mfma_scale_f32_16x16x128_f8f6f4 v[98:101], v[10:17], v[234:241], 0, v191, v191 op_sel_hi:[0,0,0]
	s_setprio 0
	s_barrier
	s_add_i32 s4, s4, s92
	v_lshl_add_u64 v[180:181], s[36:37], 0, v[162:163]
	s_mov_b32 m0, s4
	ds_read_b128 v[206:209], v201 offset:16384
	ds_read_b128 v[210:213], v201 offset:17408
	ds_read_b128 v[214:217], v201 offset:18432
	ds_read_b128 v[218:221], v201 offset:19456
	ds_read_b128 v[234:237], v201 offset:20480
	ds_read_b128 v[238:241], v201 offset:21504
	ds_read_b128 v[242:245], v201 offset:22528
	ds_read_b128 v[246:249], v201 offset:23552
	global_load_lds_dwordx4 v[180:181], off
	s_add_i32 m0, s4, 0x2000
	s_add_u32 s86, s36, 0x20000
	v_lshl_add_u64 v[182:183], s[36:37], 0, v[164:165]
	s_addc_u32 s87, s37, 0
	s_add_i32 s4, s69, s92
	global_load_lds_dwordx4 v[182:183], off
	v_lshl_add_u64 v[184:185], s[86:87], 0, v[162:163]
	s_mov_b32 m0, s4
	v_cndmask_b32_e32 v0, v168, v202, vcc
	global_load_lds_dwordx4 v[184:185], off
	v_lshl_add_u64 v[184:185], s[86:87], 0, v[164:165]
	s_add_i32 m0, s4, 0x2000
	v_lshl_add_u64 v[186:187], s[70:71], 0, v[0:1]
	global_load_lds_dwordx4 v[184:185], off
	s_mov_b32 m0, s93
	v_cndmask_b32_e32 v184, v170, v203, vcc
	global_load_lds_dwordx4 v0, s[70:71]
	s_mov_b32 m0, s79
	v_mov_b32_e32 v185, v1
	global_load_lds_dwordx4 v184, s[70:71]
	s_waitcnt vmcnt(8)
	s_waitcnt lgkmcnt(0)
	v_lshl_add_u64 v[184:185], s[70:71], 0, v[184:185]
	s_barrier
	s_setprio 1
	s_waitcnt lgkmcnt(0)
	v_mfma_scale_f32_16x16x128_f8f6f4 v[94:97], v[18:25], v[206:213], 0, v191, v191 op_sel_hi:[0,0,0]
	v_mfma_scale_f32_16x16x128_f8f6f4 v[90:93], v[26:33], v[206:213], 0, v191, v191 op_sel_hi:[0,0,0]
	v_mfma_scale_f32_16x16x128_f8f6f4 v[70:73], v[18:25], v[214:221], 0, v191, v191 op_sel_hi:[0,0,0]
	v_mfma_scale_f32_16x16x128_f8f6f4 v[66:69], v[26:33], v[214:221], 0, v191, v191 op_sel_hi:[0,0,0]
	v_mfma_scale_f32_16x16x128_f8f6f4 v[54:57], v[18:25], v[234:241], 0, v191, v191 op_sel_hi:[0,0,0]
	v_mfma_scale_f32_16x16x128_f8f6f4 v[50:53], v[26:33], v[234:241], 0, v191, v191 op_sel_hi:[0,0,0]
	v_mfma_scale_f32_16x16x128_f8f6f4 v[38:41], v[18:25], v[242:249], 0, v191, v191 op_sel_hi:[0,0,0]
	v_mfma_scale_f32_16x16x128_f8f6f4 v[34:37], v[26:33], v[242:249], 0, v191, v191 op_sel_hi:[0,0,0]
	s_setprio 0
	s_setprio 1
	v_mfma_scale_f32_16x16x128_f8f6f4 v[86:89], v[2:9], v[206:213], 0, v191, v191 op_sel_hi:[0,0,0]
	v_mfma_scale_f32_16x16x128_f8f6f4 v[82:85], v[10:17], v[206:213], 0, v191, v191 op_sel_hi:[0,0,0]
	v_mfma_scale_f32_16x16x128_f8f6f4 v[78:81], v[2:9], v[214:221], 0, v191, v191 op_sel_hi:[0,0,0]
	v_mfma_scale_f32_16x16x128_f8f6f4 v[74:77], v[10:17], v[214:221], 0, v191, v191 op_sel_hi:[0,0,0]
	v_mfma_scale_f32_16x16x128_f8f6f4 v[62:65], v[2:9], v[234:241], 0, v191, v191 op_sel_hi:[0,0,0]
	v_mfma_scale_f32_16x16x128_f8f6f4 v[58:61], v[10:17], v[234:241], 0, v191, v191 op_sel_hi:[0,0,0]
	v_mfma_scale_f32_16x16x128_f8f6f4 v[46:49], v[2:9], v[242:249], 0, v191, v191 op_sel_hi:[0,0,0]
	v_mfma_scale_f32_16x16x128_f8f6f4 v[42:45], v[10:17], v[242:249], 0, v191, v191 op_sel_hi:[0,0,0]
	s_setprio 0
	s_barrier
	s_add_i32 s4, 0, 0x18000
	v_add_u32_e32 v0, s4, v200
	s_add_i32 s69, 0, 0x1c000
	ds_read_b128 v[2:5], v0
	ds_read_b128 v[6:9], v0 offset:1024
	ds_read_b128 v[10:13], v0 offset:2048
	ds_read_b128 v[14:17], v0 offset:3072
	v_add_u32_e32 v0, s69, v200
	ds_read_b128 v[18:21], v0
	ds_read_b128 v[22:25], v0 offset:1024
	ds_read_b128 v[26:29], v0 offset:2048
	ds_read_b128 v[30:33], v0 offset:3072
	s_mov_b32 m0, s84
	v_cndmask_b32_e32 v0, v172, v204, vcc
	ds_read_b128 v[206:209], v201 offset:32768
	ds_read_b128 v[210:213], v201 offset:33792
	ds_read_b128 v[214:217], v201 offset:34816
	ds_read_b128 v[218:221], v201 offset:35840
	ds_read_b128 v[234:237], v201 offset:36864
	ds_read_b128 v[238:241], v201 offset:37888
	ds_read_b128 v[242:245], v201 offset:38912
	ds_read_b128 v[246:249], v201 offset:39936
	v_cndmask_b32_e32 v173, v174, v205, vcc
	global_load_lds_dwordx4 v0, s[70:71]
	s_mov_b32 m0, s85
	s_nop 0
	global_load_lds_dwordx4 v173, s[70:71]
	s_waitcnt vmcnt(8)
	s_waitcnt lgkmcnt(0)
	s_barrier
	s_setprio 1
	s_waitcnt lgkmcnt(0)
	v_mfma_scale_f32_16x16x128_f8f6f4 v[158:161], v[2:9], v[206:213], v[158:161], v191, v191 op_sel_hi:[0,0,0]
	v_mfma_scale_f32_16x16x128_f8f6f4 v[154:157], v[10:17], v[206:213], v[154:157], v191, v191 op_sel_hi:[0,0,0]
	v_mfma_scale_f32_16x16x128_f8f6f4 v[142:145], v[2:9], v[214:221], v[142:145], v191, v191 op_sel_hi:[0,0,0]
	v_mfma_scale_f32_16x16x128_f8f6f4 v[138:141], v[10:17], v[214:221], v[138:141], v191, v191 op_sel_hi:[0,0,0]
	v_mfma_scale_f32_16x16x128_f8f6f4 v[126:129], v[2:9], v[234:241], v[126:129], v191, v191 op_sel_hi:[0,0,0]
	v_mfma_scale_f32_16x16x128_f8f6f4 v[122:125], v[10:17], v[234:241], v[122:125], v191, v191 op_sel_hi:[0,0,0]
	v_mfma_scale_f32_16x16x128_f8f6f4 v[110:113], v[2:9], v[242:249], v[110:113], v191, v191 op_sel_hi:[0,0,0]
	v_mfma_scale_f32_16x16x128_f8f6f4 v[106:109], v[10:17], v[242:249], v[106:109], v191, v191 op_sel_hi:[0,0,0]
	s_setprio 0
	s_setprio 1
	v_mfma_scale_f32_16x16x128_f8f6f4 v[150:153], v[18:25], v[206:213], v[150:153], v191, v191 op_sel_hi:[0,0,0]
	v_mfma_scale_f32_16x16x128_f8f6f4 v[146:149], v[26:33], v[206:213], v[146:149], v191, v191 op_sel_hi:[0,0,0]
	v_mfma_scale_f32_16x16x128_f8f6f4 v[134:137], v[18:25], v[214:221], v[134:137], v191, v191 op_sel_hi:[0,0,0]
	v_mfma_scale_f32_16x16x128_f8f6f4 v[130:133], v[26:33], v[214:221], v[130:133], v191, v191 op_sel_hi:[0,0,0]
	v_mfma_scale_f32_16x16x128_f8f6f4 v[118:121], v[18:25], v[234:241], v[118:121], v191, v191 op_sel_hi:[0,0,0]
	v_mfma_scale_f32_16x16x128_f8f6f4 v[114:117], v[26:33], v[234:241], v[114:117], v191, v191 op_sel_hi:[0,0,0]
	v_mfma_scale_f32_16x16x128_f8f6f4 v[102:105], v[18:25], v[242:249], v[102:105], v191, v191 op_sel_hi:[0,0,0]
	v_mfma_scale_f32_16x16x128_f8f6f4 v[98:101], v[26:33], v[242:249], v[98:101], v191, v191 op_sel_hi:[0,0,0]
	s_setprio 0
	s_barrier
	s_add_i32 s4, s4, s92
	v_lshl_add_u64 v[180:181], v[180:181], 0, s[22:23]
	s_mov_b32 m0, s4
	ds_read_b128 v[206:209], v201 offset:49152
	ds_read_b128 v[210:213], v201 offset:50176
	ds_read_b128 v[214:217], v201 offset:51200
	ds_read_b128 v[218:221], v201 offset:52224
	ds_read_b128 v[234:237], v201 offset:53248
	ds_read_b128 v[238:241], v201 offset:54272
	ds_read_b128 v[242:245], v201 offset:55296
	ds_read_b128 v[246:249], v201 offset:56320
	global_load_lds_dwordx4 v[180:181], off
	s_add_i32 m0, s4, 0x2000
	s_add_u32 s36, s36, 0x20080
	v_lshl_add_u64 v[180:181], v[182:183], 0, s[22:23]
	s_addc_u32 s37, s37, 0
	s_add_i32 s4, s69, s92
	global_load_lds_dwordx4 v[180:181], off
	v_lshl_add_u64 v[180:181], s[36:37], 0, v[162:163]
	s_mov_b32 m0, s4
	s_nop 0
	global_load_lds_dwordx4 v[180:181], off
	v_lshl_add_u64 v[180:181], s[36:37], 0, v[164:165]
	s_add_i32 m0, s4, 0x2000
	s_nop 0
	global_load_lds_dwordx4 v[180:181], off
	v_lshl_add_u64 v[180:181], v[186:187], 0, s[22:23]
	s_mov_b32 m0, s15
	s_nop 0
	global_load_lds_dwordx4 v[180:181], off
	v_lshl_add_u64 v[180:181], v[184:185], 0, s[22:23]
	s_mov_b32 m0, s16
	s_nop 0
	global_load_lds_dwordx4 v[180:181], off
	s_waitcnt vmcnt(8)
	s_waitcnt lgkmcnt(0)
	s_barrier
	s_setprio 1
	s_waitcnt lgkmcnt(0)
	v_mfma_scale_f32_16x16x128_f8f6f4 v[94:97], v[2:9], v[206:213], v[94:97], v191, v191 op_sel_hi:[0,0,0]
	v_mfma_scale_f32_16x16x128_f8f6f4 v[90:93], v[10:17], v[206:213], v[90:93], v191, v191 op_sel_hi:[0,0,0]
	v_mfma_scale_f32_16x16x128_f8f6f4 v[70:73], v[2:9], v[214:221], v[70:73], v191, v191 op_sel_hi:[0,0,0]
	v_mfma_scale_f32_16x16x128_f8f6f4 v[66:69], v[10:17], v[214:221], v[66:69], v191, v191 op_sel_hi:[0,0,0]
	v_mfma_scale_f32_16x16x128_f8f6f4 v[54:57], v[2:9], v[234:241], v[54:57], v191, v191 op_sel_hi:[0,0,0]
	v_mfma_scale_f32_16x16x128_f8f6f4 v[50:53], v[10:17], v[234:241], v[50:53], v191, v191 op_sel_hi:[0,0,0]
	v_mfma_scale_f32_16x16x128_f8f6f4 v[38:41], v[2:9], v[242:249], v[38:41], v191, v191 op_sel_hi:[0,0,0]
	v_mfma_scale_f32_16x16x128_f8f6f4 v[34:37], v[10:17], v[242:249], v[34:37], v191, v191 op_sel_hi:[0,0,0]
	s_setprio 0
	s_setprio 1
	v_mfma_scale_f32_16x16x128_f8f6f4 v[86:89], v[18:25], v[206:213], v[86:89], v191, v191 op_sel_hi:[0,0,0]
	v_mfma_scale_f32_16x16x128_f8f6f4 v[82:85], v[26:33], v[206:213], v[82:85], v191, v191 op_sel_hi:[0,0,0]
	v_mfma_scale_f32_16x16x128_f8f6f4 v[78:81], v[18:25], v[214:221], v[78:81], v191, v191 op_sel_hi:[0,0,0]
	v_mfma_scale_f32_16x16x128_f8f6f4 v[74:77], v[26:33], v[214:221], v[74:77], v191, v191 op_sel_hi:[0,0,0]
	v_mfma_scale_f32_16x16x128_f8f6f4 v[62:65], v[18:25], v[234:241], v[62:65], v191, v191 op_sel_hi:[0,0,0]
	v_mfma_scale_f32_16x16x128_f8f6f4 v[58:61], v[26:33], v[234:241], v[58:61], v191, v191 op_sel_hi:[0,0,0]
	v_mfma_scale_f32_16x16x128_f8f6f4 v[46:49], v[18:25], v[242:249], v[46:49], v191, v191 op_sel_hi:[0,0,0]
	v_mfma_scale_f32_16x16x128_f8f6f4 v[42:45], v[26:33], v[242:249], v[42:45], v191, v191 op_sel_hi:[0,0,0]
	s_setprio 0
	s_barrier
	s_add_i32 s67, s67, 2
	s_add_u32 s26, s26, 0x100
	s_addc_u32 s27, s27, 0
